# M2 epilogue: stores issued per row group again (exec-masked, fixed 16 per wave), no vmcnt(0) in the epilogue; first-iteration waits of the next unit retire the staged tiles by count (vmcnt 28)
# baseline (speedup 1.0000x reference)
.Lrelaxw_m2_0:
	s_waitcnt vmcnt(28)
	s_waitcnt lgkmcnt(0)
	s_barrier
	s_setprio 1
	s_waitcnt lgkmcnt(0)
	v_mfma_f32_16x16x32_bf16 v[136:139], v[142:145], v[192:195], v[136:139]
	v_mfma_f32_16x16x32_bf16 v[132:135], v[150:153], v[192:195], v[132:135]
	v_mfma_f32_16x16x32_bf16 v[120:123], v[142:145], v[200:203], v[120:123]
	v_mfma_f32_16x16x32_bf16 v[116:119], v[150:153], v[200:203], v[116:119]
	v_mfma_f32_16x16x32_bf16 v[104:107], v[142:145], v[208:211], v[104:107]
	v_mfma_f32_16x16x32_bf16 v[100:103], v[150:153], v[208:211], v[100:103]
	v_mfma_f32_16x16x32_bf16 v[84:87], v[142:145], v[226:229], v[84:87]
	v_mfma_f32_16x16x32_bf16 v[80:83], v[150:153], v[226:229], v[80:83]
	v_mfma_f32_16x16x32_bf16 v[136:139], v[146:149], v[196:199], v[136:139]
	v_mfma_f32_16x16x32_bf16 v[132:135], v[166:169], v[196:199], v[132:135]
	v_mfma_f32_16x16x32_bf16 v[120:123], v[146:149], v[204:207], v[120:123]
	v_mfma_f32_16x16x32_bf16 v[116:119], v[166:169], v[204:207], v[116:119]
	v_mfma_f32_16x16x32_bf16 v[104:107], v[146:149], v[218:221], v[104:107]
	v_mfma_f32_16x16x32_bf16 v[100:103], v[166:169], v[218:221], v[100:103]
	v_mfma_f32_16x16x32_bf16 v[84:87], v[146:149], v[230:233], v[84:87]
	v_mfma_f32_16x16x32_bf16 v[80:83], v[166:169], v[230:233], v[80:83]
	s_setprio 0
	s_setprio 1
	v_mfma_f32_16x16x32_bf16 v[128:131], v[170:173], v[192:195], v[128:131]
	v_mfma_f32_16x16x32_bf16 v[124:127], v[184:187], v[192:195], v[124:127]
	v_mfma_f32_16x16x32_bf16 v[112:115], v[170:173], v[200:203], v[112:115]
	v_mfma_f32_16x16x32_bf16 v[108:111], v[184:187], v[200:203], v[108:111]
	v_mfma_f32_16x16x32_bf16 v[92:95], v[170:173], v[208:211], v[92:95]
	v_mfma_f32_16x16x32_bf16 v[88:91], v[184:187], v[208:211], v[88:91]
	v_mfma_f32_16x16x32_bf16 v[76:79], v[170:173], v[226:229], v[76:79]
	v_mfma_f32_16x16x32_bf16 v[72:75], v[184:187], v[226:229], v[72:75]
	v_mfma_f32_16x16x32_bf16 v[128:131], v[174:177], v[196:199], v[128:131]
	v_mfma_f32_16x16x32_bf16 v[124:127], v[188:191], v[196:199], v[124:127]
	v_mfma_f32_16x16x32_bf16 v[112:115], v[174:177], v[204:207], v[112:115]
	v_mfma_f32_16x16x32_bf16 v[108:111], v[188:191], v[204:207], v[108:111]
	v_mfma_f32_16x16x32_bf16 v[92:95], v[174:177], v[218:221], v[92:95]
	v_mfma_f32_16x16x32_bf16 v[88:91], v[188:191], v[218:221], v[88:91]
	v_mfma_f32_16x16x32_bf16 v[76:79], v[174:177], v[230:233], v[76:79]
	v_mfma_f32_16x16x32_bf16 v[72:75], v[188:191], v[230:233], v[72:75]
	s_setprio 0
	s_barrier
	s_add_i32 s22, s22, s24
	v_lshl_add_u64 v[154:155], s[44:45], 0, v[96:97]
	s_mov_b32 m0, s22
	ds_read_b128 v[192:195], v165 offset:16384
	ds_read_b128 v[196:199], v165 offset:17408
	ds_read_b128 v[200:203], v165 offset:18432
	ds_read_b128 v[204:207], v165 offset:19456
	ds_read_b128 v[208:211], v165 offset:20480
	ds_read_b128 v[218:221], v165 offset:21504
	ds_read_b128 v[226:229], v165 offset:22528
	ds_read_b128 v[230:233], v165 offset:23552
	global_load_lds_dwordx4 v[154:155], off
	s_add_i32 m0, s22, 0x2000
	s_add_u32 s40, s44, 0x40000
	v_lshl_add_u64 v[178:179], s[44:45], 0, v[156:157]
	s_addc_u32 s41, s45, 0
	s_add_i32 s22, s28, s24
	global_load_lds_dwordx4 v[178:179], off
	v_lshl_add_u64 v[180:181], s[40:41], 0, v[96:97]
	s_mov_b32 m0, s22
	s_nop 0
	global_load_lds_dwordx4 v[180:181], off
	v_lshl_add_u64 v[180:181], s[40:41], 0, v[156:157]
	s_add_i32 m0, s22, 0x2000
	s_and_b64 s[40:41], s[18:19], s[46:47]
	s_and_b64 s[40:41], s[40:41], exec
	s_cselect_b32 s28, s34, s38
	s_cselect_b32 s22, s35, s39
	s_add_u32 s40, s28, s58
	s_addc_u32 s41, s22, 0
	global_load_lds_dwordx4 v[180:181], off
	v_lshl_add_u64 v[180:181], s[40:41], 0, v[96:97]
	s_mov_b32 m0, s50
	v_lshl_add_u64 v[182:183], s[40:41], 0, v[156:157]
	global_load_lds_dwordx4 v[180:181], off
	s_mov_b32 m0, s51
	s_nop 0
	global_load_lds_dwordx4 v[182:183], off
	s_cmp_lg_u32 s100, 0
	s_cbranch_scc1 .Lrelaxw_m2_1
	s_waitcnt vmcnt(8)
.Lrelaxw_m2_1:
	s_waitcnt vmcnt(28)
	s_waitcnt lgkmcnt(0)
	s_barrier
	s_setprio 1
	s_waitcnt lgkmcnt(0)
	v_mfma_f32_16x16x32_bf16 v[68:71], v[142:145], v[192:195], v[68:71]
	v_mfma_f32_16x16x32_bf16 v[64:67], v[150:153], v[192:195], v[64:67]
	v_mfma_f32_16x16x32_bf16 v[52:55], v[142:145], v[200:203], v[52:55]
	v_mfma_f32_16x16x32_bf16 v[48:51], v[150:153], v[200:203], v[48:51]
	v_mfma_f32_16x16x32_bf16 v[36:39], v[142:145], v[208:211], v[36:39]
	v_mfma_f32_16x16x32_bf16 v[32:35], v[150:153], v[208:211], v[32:35]
	v_mfma_f32_16x16x32_bf16 v[18:21], v[142:145], v[226:229], v[18:21]
	v_mfma_f32_16x16x32_bf16 v[14:17], v[150:153], v[226:229], v[14:17]
	v_mfma_f32_16x16x32_bf16 v[68:71], v[146:149], v[196:199], v[68:71]
	v_mfma_f32_16x16x32_bf16 v[64:67], v[166:169], v[196:199], v[64:67]
	v_mfma_f32_16x16x32_bf16 v[52:55], v[146:149], v[204:207], v[52:55]
	v_mfma_f32_16x16x32_bf16 v[48:51], v[166:169], v[204:207], v[48:51]
	v_mfma_f32_16x16x32_bf16 v[36:39], v[146:149], v[218:221], v[36:39]
	v_mfma_f32_16x16x32_bf16 v[32:35], v[166:169], v[218:221], v[32:35]
	v_mfma_f32_16x16x32_bf16 v[18:21], v[146:149], v[230:233], v[18:21]
	v_mfma_f32_16x16x32_bf16 v[14:17], v[166:169], v[230:233], v[14:17]
	s_setprio 0
	s_setprio 1
	v_mfma_f32_16x16x32_bf16 v[60:63], v[170:173], v[192:195], v[60:63]
	v_mfma_f32_16x16x32_bf16 v[56:59], v[184:187], v[192:195], v[56:59]
	v_mfma_f32_16x16x32_bf16 v[44:47], v[170:173], v[200:203], v[44:47]
	v_mfma_f32_16x16x32_bf16 v[40:43], v[184:187], v[200:203], v[40:43]
	v_mfma_f32_16x16x32_bf16 v[28:31], v[170:173], v[208:211], v[28:31]
	v_mfma_f32_16x16x32_bf16 v[24:27], v[184:187], v[208:211], v[24:27]
	v_mfma_f32_16x16x32_bf16 v[10:13], v[170:173], v[226:229], v[10:13]
	v_mfma_f32_16x16x32_bf16 v[6:9], v[184:187], v[226:229], v[6:9]
	v_mfma_f32_16x16x32_bf16 v[60:63], v[174:177], v[196:199], v[60:63]
	v_mfma_f32_16x16x32_bf16 v[56:59], v[188:191], v[196:199], v[56:59]
	v_mfma_f32_16x16x32_bf16 v[44:47], v[174:177], v[204:207], v[44:47]
	v_mfma_f32_16x16x32_bf16 v[40:43], v[188:191], v[204:207], v[40:43]
	v_mfma_f32_16x16x32_bf16 v[28:31], v[174:177], v[218:221], v[28:31]
	v_mfma_f32_16x16x32_bf16 v[24:27], v[188:191], v[218:221], v[24:27]
	v_mfma_f32_16x16x32_bf16 v[10:13], v[174:177], v[230:233], v[10:13]
	v_mfma_f32_16x16x32_bf16 v[6:9], v[188:191], v[230:233], v[6:9]
	s_setprio 0
	s_barrier
	s_add_i32 s22, 0, 0x18000
	v_add_u32_e32 v98, s22, v162
	s_add_i32 s28, 0, 0x1c000
	ds_read_b128 v[142:145], v98
	ds_read_b128 v[146:149], v98 offset:1024
	ds_read_b128 v[150:153], v98 offset:2048
	ds_read_b128 v[166:169], v98 offset:3072
	v_add_u32_e32 v98, s28, v162
	ds_read_b128 v[170:173], v98
	ds_read_b128 v[174:177], v98 offset:1024
	ds_read_b128 v[184:187], v98 offset:2048
	ds_read_b128 v[188:191], v98 offset:3072
	s_add_u32 s40, s40, 0x40000
	s_addc_u32 s41, s41, 0
	s_mov_b32 m0, s52
	v_lshl_add_u64 v[212:213], s[40:41], 0, v[96:97]
	ds_read_b128 v[192:195], v165 offset:32768
	ds_read_b128 v[196:199], v165 offset:33792
	ds_read_b128 v[200:203], v165 offset:34816
	ds_read_b128 v[204:207], v165 offset:35840
	ds_read_b128 v[208:211], v165 offset:36864
	ds_read_b128 v[218:221], v165 offset:37888
	ds_read_b128 v[226:229], v165 offset:38912
	ds_read_b128 v[230:233], v165 offset:39936
	global_load_lds_dwordx4 v[212:213], off
	v_lshl_add_u64 v[212:213], s[40:41], 0, v[156:157]
	s_mov_b32 m0, s53
	s_nop 0
	global_load_lds_dwordx4 v[212:213], off
	s_waitcnt vmcnt(8)
	s_waitcnt lgkmcnt(0)
	s_barrier
	s_setprio 1
	s_waitcnt lgkmcnt(0)
	v_mfma_f32_16x16x32_bf16 v[136:139], v[142:145], v[192:195], v[136:139]
	v_mfma_f32_16x16x32_bf16 v[132:135], v[150:153], v[192:195], v[132:135]
	v_mfma_f32_16x16x32_bf16 v[120:123], v[142:145], v[200:203], v[120:123]
	v_mfma_f32_16x16x32_bf16 v[116:119], v[150:153], v[200:203], v[116:119]
	v_mfma_f32_16x16x32_bf16 v[104:107], v[142:145], v[208:211], v[104:107]
	v_mfma_f32_16x16x32_bf16 v[100:103], v[150:153], v[208:211], v[100:103]
	v_mfma_f32_16x16x32_bf16 v[84:87], v[142:145], v[226:229], v[84:87]
	v_mfma_f32_16x16x32_bf16 v[80:83], v[150:153], v[226:229], v[80:83]
	v_mfma_f32_16x16x32_bf16 v[136:139], v[146:149], v[196:199], v[136:139]
	v_mfma_f32_16x16x32_bf16 v[132:135], v[166:169], v[196:199], v[132:135]
	v_mfma_f32_16x16x32_bf16 v[120:123], v[146:149], v[204:207], v[120:123]
	v_mfma_f32_16x16x32_bf16 v[116:119], v[166:169], v[204:207], v[116:119]
	v_mfma_f32_16x16x32_bf16 v[104:107], v[146:149], v[218:221], v[104:107]
	v_mfma_f32_16x16x32_bf16 v[100:103], v[166:169], v[218:221], v[100:103]
	v_mfma_f32_16x16x32_bf16 v[84:87], v[146:149], v[230:233], v[84:87]
	v_mfma_f32_16x16x32_bf16 v[80:83], v[166:169], v[230:233], v[80:83]
	s_setprio 0
	s_setprio 1
	v_mfma_f32_16x16x32_bf16 v[128:131], v[170:173], v[192:195], v[128:131]
	v_mfma_f32_16x16x32_bf16 v[124:127], v[184:187], v[192:195], v[124:127]
	v_mfma_f32_16x16x32_bf16 v[112:115], v[170:173], v[200:203], v[112:115]
	v_mfma_f32_16x16x32_bf16 v[108:111], v[184:187], v[200:203], v[108:111]
	v_mfma_f32_16x16x32_bf16 v[92:95], v[170:173], v[208:211], v[92:95]
	v_mfma_f32_16x16x32_bf16 v[88:91], v[184:187], v[208:211], v[88:91]
	v_mfma_f32_16x16x32_bf16 v[76:79], v[170:173], v[226:229], v[76:79]
	v_mfma_f32_16x16x32_bf16 v[72:75], v[184:187], v[226:229], v[72:75]
	v_mfma_f32_16x16x32_bf16 v[128:131], v[174:177], v[196:199], v[128:131]
	v_mfma_f32_16x16x32_bf16 v[124:127], v[188:191], v[196:199], v[124:127]
	v_mfma_f32_16x16x32_bf16 v[112:115], v[174:177], v[204:207], v[112:115]
	v_mfma_f32_16x16x32_bf16 v[108:111], v[188:191], v[204:207], v[108:111]
	v_mfma_f32_16x16x32_bf16 v[92:95], v[174:177], v[218:221], v[92:95]
	v_mfma_f32_16x16x32_bf16 v[88:91], v[188:191], v[218:221], v[88:91]
	v_mfma_f32_16x16x32_bf16 v[76:79], v[174:177], v[230:233], v[76:79]
	v_mfma_f32_16x16x32_bf16 v[72:75], v[188:191], v[230:233], v[72:75]
	s_setprio 0
	s_barrier
	s_add_i32 s22, s22, s24
	v_lshl_add_u64 v[154:155], v[154:155], 0, s[0:1]
	s_mov_b32 m0, s22
	ds_read_b128 v[192:195], v165 offset:49152
	ds_read_b128 v[196:199], v165 offset:50176
	ds_read_b128 v[200:203], v165 offset:51200
	ds_read_b128 v[204:207], v165 offset:52224
	ds_read_b128 v[208:211], v165 offset:53248
	ds_read_b128 v[218:221], v165 offset:54272
	ds_read_b128 v[226:229], v165 offset:55296
	ds_read_b128 v[230:233], v165 offset:56320
	global_load_lds_dwordx4 v[154:155], off
	s_add_i32 m0, s22, 0x2000
	s_add_u32 s40, s44, 0x40080
	v_lshl_add_u64 v[154:155], v[178:179], 0, s[0:1]
	s_addc_u32 s41, s45, 0
	s_add_i32 s22, s28, s24
	global_load_lds_dwordx4 v[154:155], off
	v_lshl_add_u64 v[154:155], s[40:41], 0, v[96:97]
	s_mov_b32 m0, s22
	s_nop 0
	global_load_lds_dwordx4 v[154:155], off
	v_lshl_add_u64 v[154:155], s[40:41], 0, v[156:157]
	s_add_i32 m0, s22, 0x2000
	s_nop 0
	global_load_lds_dwordx4 v[154:155], off
	v_lshl_add_u64 v[154:155], v[180:181], 0, s[0:1]
	s_mov_b32 m0, s4
	s_nop 0
	global_load_lds_dwordx4 v[154:155], off
	v_lshl_add_u64 v[154:155], v[182:183], 0, s[0:1]
	s_mov_b32 m0, s54
	s_nop 0
	global_load_lds_dwordx4 v[154:155], off
	s_waitcnt vmcnt(8)
	s_waitcnt lgkmcnt(0)
	s_barrier
	s_setprio 1
	s_waitcnt lgkmcnt(0)
	v_mfma_f32_16x16x32_bf16 v[68:71], v[142:145], v[192:195], v[68:71]
	v_mfma_f32_16x16x32_bf16 v[64:67], v[150:153], v[192:195], v[64:67]
	v_mfma_f32_16x16x32_bf16 v[52:55], v[142:145], v[200:203], v[52:55]
	v_mfma_f32_16x16x32_bf16 v[48:51], v[150:153], v[200:203], v[48:51]
	v_mfma_f32_16x16x32_bf16 v[36:39], v[142:145], v[208:211], v[36:39]
	v_mfma_f32_16x16x32_bf16 v[32:35], v[150:153], v[208:211], v[32:35]
	v_mfma_f32_16x16x32_bf16 v[18:21], v[142:145], v[226:229], v[18:21]
	v_mfma_f32_16x16x32_bf16 v[14:17], v[150:153], v[226:229], v[14:17]
	v_mfma_f32_16x16x32_bf16 v[68:71], v[146:149], v[196:199], v[68:71]
	v_mfma_f32_16x16x32_bf16 v[64:67], v[166:169], v[196:199], v[64:67]
	v_mfma_f32_16x16x32_bf16 v[52:55], v[146:149], v[204:207], v[52:55]
	v_mfma_f32_16x16x32_bf16 v[48:51], v[166:169], v[204:207], v[48:51]
	v_mfma_f32_16x16x32_bf16 v[36:39], v[146:149], v[218:221], v[36:39]
	v_mfma_f32_16x16x32_bf16 v[32:35], v[166:169], v[218:221], v[32:35]
	v_mfma_f32_16x16x32_bf16 v[18:21], v[146:149], v[230:233], v[18:21]
	v_mfma_f32_16x16x32_bf16 v[14:17], v[166:169], v[230:233], v[14:17]
	s_setprio 0
	s_setprio 1
	v_mfma_f32_16x16x32_bf16 v[60:63], v[170:173], v[192:195], v[60:63]
	v_mfma_f32_16x16x32_bf16 v[56:59], v[184:187], v[192:195], v[56:59]
	v_mfma_f32_16x16x32_bf16 v[44:47], v[170:173], v[200:203], v[44:47]
	v_mfma_f32_16x16x32_bf16 v[40:43], v[184:187], v[200:203], v[40:43]
	v_mfma_f32_16x16x32_bf16 v[28:31], v[170:173], v[208:211], v[28:31]
	v_mfma_f32_16x16x32_bf16 v[24:27], v[184:187], v[208:211], v[24:27]
	v_mfma_f32_16x16x32_bf16 v[10:13], v[170:173], v[226:229], v[10:13]
	v_mfma_f32_16x16x32_bf16 v[6:9], v[184:187], v[226:229], v[6:9]
	v_mfma_f32_16x16x32_bf16 v[60:63], v[174:177], v[196:199], v[60:63]
	v_mfma_f32_16x16x32_bf16 v[56:59], v[188:191], v[196:199], v[56:59]
	v_mfma_f32_16x16x32_bf16 v[44:47], v[174:177], v[204:207], v[44:47]
	v_mfma_f32_16x16x32_bf16 v[40:43], v[188:191], v[204:207], v[40:43]
	v_mfma_f32_16x16x32_bf16 v[28:31], v[174:177], v[218:221], v[28:31]
	v_mfma_f32_16x16x32_bf16 v[24:27], v[188:191], v[218:221], v[24:27]
	v_mfma_f32_16x16x32_bf16 v[10:13], v[174:177], v[230:233], v[10:13]
	v_mfma_f32_16x16x32_bf16 v[6:9], v[188:191], v[230:233], v[6:9]
	s_setprio 0
	s_barrier
	s_mov_b32 s100, 0
	s_add_i32 s78, s78, 2
	s_cmp_gt_u32 s78, 13
	s_mov_b64 s[40:41], s[42:43]
	s_cbranch_scc0 .LBB0_2958
	s_and_b64 vcc, exec, s[14:15]
	s_cbranch_vccz .LBB0_2961
	s_barrier
.LBB0_2961:
	v_lshl_or_b32 v2, v23, 8, v164
	s_lshl_b32 s22, s31, 10
	v_add_u32_e32 v22, s22, v163
	v_ashrrev_i32_e32 v3, 31, v2
	ds_read_b32 v176, v22
	ds_read_b32 v178, v22 offset:64
	ds_read_b32 v180, v22 offset:128
	ds_read_b32 v182, v22 offset:192
	ds_read_b32 v184, v22 offset:512
	ds_read_b32 v186, v22 offset:576
	ds_read_b32 v188, v22 offset:640
	ds_read_b32 v190, v22 offset:704
	ds_read_b32 v192, v22 offset:13568
	ds_read_b32 v194, v22 offset:13632
	ds_read_b32 v196, v22 offset:13696
	ds_read_b32 v198, v22 offset:13760
	ds_read_b32 v200, v22 offset:14080
	ds_read_b32 v202, v22 offset:14144
	ds_read_b32 v204, v22 offset:14208
	ds_read_b32 v206, v22 offset:14272
	v_mov_b32_e32 v177, v99
	v_mov_b32_e32 v179, v99
	v_mov_b32_e32 v181, v99
	v_mov_b32_e32 v183, v99
	v_mov_b32_e32 v185, v99
	v_mov_b32_e32 v187, v99
	v_mov_b32_e32 v189, v99
	v_mov_b32_e32 v191, v99
	s_waitcnt lgkmcnt(0)
	v_lshlrev_b64 v[140:141], 11, v[176:177]
	v_lshl_add_u64 v[140:141], s[12:13], 0, v[140:141]
	v_lshl_add_u64 v[140:141], v[2:3], 1, v[140:141]
	v_lshlrev_b64 v[142:143], 11, v[178:179]
	v_lshl_add_u64 v[142:143], s[12:13], 0, v[142:143]
	v_lshl_add_u64 v[142:143], v[2:3], 1, v[142:143]
	v_lshlrev_b64 v[144:145], 11, v[180:181]
	v_lshl_add_u64 v[144:145], s[12:13], 0, v[144:145]
	v_lshl_add_u64 v[144:145], v[2:3], 1, v[144:145]
	v_lshlrev_b64 v[146:147], 11, v[182:183]
	v_lshl_add_u64 v[146:147], s[12:13], 0, v[146:147]
	v_lshl_add_u64 v[146:147], v[2:3], 1, v[146:147]
	v_lshlrev_b64 v[148:149], 11, v[184:185]
	v_lshl_add_u64 v[148:149], s[12:13], 0, v[148:149]
	v_lshl_add_u64 v[148:149], v[2:3], 1, v[148:149]
	v_lshlrev_b64 v[150:151], 11, v[186:187]
	v_lshl_add_u64 v[150:151], s[12:13], 0, v[150:151]
	v_lshl_add_u64 v[150:151], v[2:3], 1, v[150:151]
	v_lshlrev_b64 v[152:153], 11, v[188:189]
	v_lshl_add_u64 v[152:153], s[12:13], 0, v[152:153]
	v_lshl_add_u64 v[152:153], v[2:3], 1, v[152:153]
	v_lshlrev_b64 v[154:155], 11, v[190:191]
	v_lshl_add_u64 v[154:155], s[12:13], 0, v[154:155]
	v_lshl_add_u64 v[154:155], v[2:3], 1, v[154:155]
	v_pk_add_f32 v[138:139], v[138:139], v[248:249]
	v_pk_add_f32 v[136:137], v[136:137], v[246:247]
	v_pk_add_f32 v[134:135], v[134:135], v[244:245]
	v_pk_add_f32 v[132:133], v[132:133], v[242:243]
	v_pk_add_f32 v[130:131], v[130:131], v[240:241]
	v_pk_add_f32 v[128:129], v[128:129], v[238:239]
	v_pk_add_f32 v[126:127], v[126:127], v[236:237]
	v_pk_add_f32 v[124:125], v[124:125], v[234:235]
	v_pk_mul_f32 v[138:139], v[138:139], v[192:193] op_sel_hi:[1,0]
	v_pk_mul_f32 v[136:137], v[136:137], v[192:193] op_sel_hi:[1,0]
	v_pk_mul_f32 v[134:135], v[134:135], v[192:193] op_sel_hi:[1,0]
	v_pk_mul_f32 v[132:133], v[132:133], v[192:193] op_sel_hi:[1,0]
	v_pk_mul_f32 v[130:131], v[130:131], v[192:193] op_sel_hi:[1,0]
	v_pk_mul_f32 v[128:129], v[128:129], v[192:193] op_sel_hi:[1,0]
	v_pk_mul_f32 v[210:211], v[126:127], v[192:193] op_sel_hi:[1,0]
	v_pk_mul_f32 v[208:209], v[124:125], v[192:193] op_sel_hi:[1,0]
	v_cvt_pk_bf16_f32 v124, v136, v137
	v_cvt_pk_bf16_f32 v125, v138, v139
	v_cvt_pk_bf16_f32 v126, v132, v133
	v_cvt_pk_bf16_f32 v127, v134, v135
	v_cvt_pk_bf16_f32 v128, v128, v129
	v_cvt_pk_bf16_f32 v129, v130, v131
	v_cvt_pk_bf16_f32 v130, v208, v209
	v_cvt_pk_bf16_f32 v131, v210, v211
	v_cmp_lt_i32_e32 vcc, -1, v176
	s_and_saveexec_b64 s[38:39], vcc
	global_store_dwordx4 v[140:141], v[124:127], off
	global_store_dwordx4 v[140:141], v[128:131], off offset:256
	s_or_b64 exec, exec, s[38:39]
	v_pk_add_f32 v[122:123], v[122:123], v[248:249]
	v_pk_add_f32 v[120:121], v[120:121], v[246:247]
	v_pk_add_f32 v[118:119], v[118:119], v[244:245]
	v_pk_add_f32 v[116:117], v[116:117], v[242:243]
	v_pk_add_f32 v[114:115], v[114:115], v[240:241]
	v_pk_add_f32 v[112:113], v[112:113], v[238:239]
	v_pk_add_f32 v[110:111], v[110:111], v[236:237]
	v_pk_add_f32 v[108:109], v[108:109], v[234:235]
	v_pk_mul_f32 v[122:123], v[122:123], v[194:195] op_sel_hi:[1,0]
	v_pk_mul_f32 v[120:121], v[120:121], v[194:195] op_sel_hi:[1,0]
	v_pk_mul_f32 v[118:119], v[118:119], v[194:195] op_sel_hi:[1,0]
	v_pk_mul_f32 v[116:117], v[116:117], v[194:195] op_sel_hi:[1,0]
	v_pk_mul_f32 v[114:115], v[114:115], v[194:195] op_sel_hi:[1,0]
	v_pk_mul_f32 v[112:113], v[112:113], v[194:195] op_sel_hi:[1,0]
	v_pk_mul_f32 v[210:211], v[110:111], v[194:195] op_sel_hi:[1,0]
	v_pk_mul_f32 v[208:209], v[108:109], v[194:195] op_sel_hi:[1,0]
	v_cvt_pk_bf16_f32 v108, v120, v121
	v_cvt_pk_bf16_f32 v109, v122, v123
	v_cvt_pk_bf16_f32 v110, v116, v117
	v_cvt_pk_bf16_f32 v111, v118, v119
	v_cvt_pk_bf16_f32 v112, v112, v113
	v_cvt_pk_bf16_f32 v113, v114, v115
	v_cvt_pk_bf16_f32 v114, v208, v209
	v_cvt_pk_bf16_f32 v115, v210, v211
	v_cmp_lt_i32_e32 vcc, -1, v178
	s_and_saveexec_b64 s[38:39], vcc
	global_store_dwordx4 v[142:143], v[108:111], off
	global_store_dwordx4 v[142:143], v[112:115], off offset:256
	s_or_b64 exec, exec, s[38:39]
	v_pk_add_f32 v[106:107], v[106:107], v[248:249]
	v_pk_add_f32 v[104:105], v[104:105], v[246:247]
	v_pk_add_f32 v[102:103], v[102:103], v[244:245]
	v_pk_add_f32 v[100:101], v[100:101], v[242:243]
	v_pk_add_f32 v[94:95], v[94:95], v[240:241]
	v_pk_add_f32 v[92:93], v[92:93], v[238:239]
	v_pk_add_f32 v[90:91], v[90:91], v[236:237]
	v_pk_add_f32 v[88:89], v[88:89], v[234:235]
	v_pk_mul_f32 v[106:107], v[106:107], v[196:197] op_sel_hi:[1,0]
	v_pk_mul_f32 v[104:105], v[104:105], v[196:197] op_sel_hi:[1,0]
	v_pk_mul_f32 v[102:103], v[102:103], v[196:197] op_sel_hi:[1,0]
	v_pk_mul_f32 v[100:101], v[100:101], v[196:197] op_sel_hi:[1,0]
	v_pk_mul_f32 v[94:95], v[94:95], v[196:197] op_sel_hi:[1,0]
	v_pk_mul_f32 v[92:93], v[92:93], v[196:197] op_sel_hi:[1,0]
	v_pk_mul_f32 v[210:211], v[90:91], v[196:197] op_sel_hi:[1,0]
	v_pk_mul_f32 v[208:209], v[88:89], v[196:197] op_sel_hi:[1,0]
	v_cvt_pk_bf16_f32 v88, v104, v105
	v_cvt_pk_bf16_f32 v89, v106, v107
	v_cvt_pk_bf16_f32 v90, v100, v101
	v_cvt_pk_bf16_f32 v91, v102, v103
	v_cvt_pk_bf16_f32 v92, v92, v93
	v_cvt_pk_bf16_f32 v93, v94, v95
	v_cvt_pk_bf16_f32 v94, v208, v209
	v_cvt_pk_bf16_f32 v95, v210, v211
	v_cmp_lt_i32_e32 vcc, -1, v180
	s_and_saveexec_b64 s[38:39], vcc
	global_store_dwordx4 v[144:145], v[88:91], off
	global_store_dwordx4 v[144:145], v[92:95], off offset:256
	s_or_b64 exec, exec, s[38:39]
	v_pk_add_f32 v[86:87], v[86:87], v[248:249]
	v_pk_add_f32 v[84:85], v[84:85], v[246:247]
	v_pk_add_f32 v[82:83], v[82:83], v[244:245]
	v_pk_add_f32 v[80:81], v[80:81], v[242:243]
	v_pk_add_f32 v[78:79], v[78:79], v[240:241]
	v_pk_add_f32 v[76:77], v[76:77], v[238:239]
	v_pk_add_f32 v[74:75], v[74:75], v[236:237]
	v_pk_add_f32 v[72:73], v[72:73], v[234:235]
	v_pk_mul_f32 v[86:87], v[86:87], v[198:199] op_sel_hi:[1,0]
	v_pk_mul_f32 v[84:85], v[84:85], v[198:199] op_sel_hi:[1,0]
	v_pk_mul_f32 v[82:83], v[82:83], v[198:199] op_sel_hi:[1,0]
	v_pk_mul_f32 v[80:81], v[80:81], v[198:199] op_sel_hi:[1,0]
	v_pk_mul_f32 v[78:79], v[78:79], v[198:199] op_sel_hi:[1,0]
	v_pk_mul_f32 v[76:77], v[76:77], v[198:199] op_sel_hi:[1,0]
	v_pk_mul_f32 v[210:211], v[74:75], v[198:199] op_sel_hi:[1,0]
	v_pk_mul_f32 v[208:209], v[72:73], v[198:199] op_sel_hi:[1,0]
	v_cvt_pk_bf16_f32 v72, v84, v85
	v_cvt_pk_bf16_f32 v73, v86, v87
	v_cvt_pk_bf16_f32 v74, v80, v81
	v_cvt_pk_bf16_f32 v75, v82, v83
	v_cvt_pk_bf16_f32 v76, v76, v77
	v_cvt_pk_bf16_f32 v77, v78, v79
	v_cvt_pk_bf16_f32 v78, v208, v209
	v_cvt_pk_bf16_f32 v79, v210, v211
	v_cmp_lt_i32_e32 vcc, -1, v182
	s_and_saveexec_b64 s[38:39], vcc
	global_store_dwordx4 v[146:147], v[72:75], off
	global_store_dwordx4 v[146:147], v[76:79], off offset:256
	s_or_b64 exec, exec, s[38:39]
	v_pk_add_f32 v[70:71], v[70:71], v[248:249]
	v_pk_add_f32 v[68:69], v[68:69], v[246:247]
	v_pk_add_f32 v[66:67], v[66:67], v[244:245]
	v_pk_add_f32 v[64:65], v[64:65], v[242:243]
	v_pk_add_f32 v[62:63], v[62:63], v[240:241]
	v_pk_add_f32 v[60:61], v[60:61], v[238:239]
	v_pk_add_f32 v[58:59], v[58:59], v[236:237]
	v_pk_add_f32 v[56:57], v[56:57], v[234:235]
	v_pk_mul_f32 v[70:71], v[70:71], v[200:201] op_sel_hi:[1,0]
	v_pk_mul_f32 v[68:69], v[68:69], v[200:201] op_sel_hi:[1,0]
	v_pk_mul_f32 v[66:67], v[66:67], v[200:201] op_sel_hi:[1,0]
	v_pk_mul_f32 v[64:65], v[64:65], v[200:201] op_sel_hi:[1,0]
	v_pk_mul_f32 v[62:63], v[62:63], v[200:201] op_sel_hi:[1,0]
	v_pk_mul_f32 v[60:61], v[60:61], v[200:201] op_sel_hi:[1,0]
	v_pk_mul_f32 v[210:211], v[58:59], v[200:201] op_sel_hi:[1,0]
	v_pk_mul_f32 v[208:209], v[56:57], v[200:201] op_sel_hi:[1,0]
	v_cvt_pk_bf16_f32 v56, v68, v69
	v_cvt_pk_bf16_f32 v57, v70, v71
	v_cvt_pk_bf16_f32 v58, v64, v65
	v_cvt_pk_bf16_f32 v59, v66, v67
	v_cvt_pk_bf16_f32 v60, v60, v61
	v_cvt_pk_bf16_f32 v61, v62, v63
	v_cvt_pk_bf16_f32 v62, v208, v209
	v_cvt_pk_bf16_f32 v63, v210, v211
	v_cmp_lt_i32_e32 vcc, -1, v184
	s_and_saveexec_b64 s[38:39], vcc
	global_store_dwordx4 v[148:149], v[56:59], off
	global_store_dwordx4 v[148:149], v[60:63], off offset:256
	s_or_b64 exec, exec, s[38:39]
	v_pk_add_f32 v[54:55], v[54:55], v[248:249]
	v_pk_add_f32 v[52:53], v[52:53], v[246:247]
	v_pk_add_f32 v[50:51], v[50:51], v[244:245]
	v_pk_add_f32 v[48:49], v[48:49], v[242:243]
	v_pk_add_f32 v[46:47], v[46:47], v[240:241]
	v_pk_add_f32 v[44:45], v[44:45], v[238:239]
	v_pk_add_f32 v[42:43], v[42:43], v[236:237]
	v_pk_add_f32 v[40:41], v[40:41], v[234:235]
	v_pk_mul_f32 v[54:55], v[54:55], v[202:203] op_sel_hi:[1,0]
	v_pk_mul_f32 v[52:53], v[52:53], v[202:203] op_sel_hi:[1,0]
	v_pk_mul_f32 v[50:51], v[50:51], v[202:203] op_sel_hi:[1,0]
	v_pk_mul_f32 v[48:49], v[48:49], v[202:203] op_sel_hi:[1,0]
	v_pk_mul_f32 v[46:47], v[46:47], v[202:203] op_sel_hi:[1,0]
	v_pk_mul_f32 v[44:45], v[44:45], v[202:203] op_sel_hi:[1,0]
	v_pk_mul_f32 v[210:211], v[42:43], v[202:203] op_sel_hi:[1,0]
	v_pk_mul_f32 v[208:209], v[40:41], v[202:203] op_sel_hi:[1,0]
	v_cvt_pk_bf16_f32 v40, v52, v53
	v_cvt_pk_bf16_f32 v41, v54, v55
	v_cvt_pk_bf16_f32 v42, v48, v49
	v_cvt_pk_bf16_f32 v43, v50, v51
	v_cvt_pk_bf16_f32 v44, v44, v45
	v_cvt_pk_bf16_f32 v45, v46, v47
	v_cvt_pk_bf16_f32 v46, v208, v209
	v_cvt_pk_bf16_f32 v47, v210, v211
	v_cmp_lt_i32_e32 vcc, -1, v186
	s_and_saveexec_b64 s[38:39], vcc
	global_store_dwordx4 v[150:151], v[40:43], off
	global_store_dwordx4 v[150:151], v[44:47], off offset:256
	s_or_b64 exec, exec, s[38:39]
	v_pk_add_f32 v[38:39], v[38:39], v[248:249]
	v_pk_add_f32 v[36:37], v[36:37], v[246:247]
	v_pk_add_f32 v[34:35], v[34:35], v[244:245]
	v_pk_add_f32 v[32:33], v[32:33], v[242:243]
	v_pk_add_f32 v[30:31], v[30:31], v[240:241]
	v_pk_add_f32 v[28:29], v[28:29], v[238:239]
	v_pk_add_f32 v[26:27], v[26:27], v[236:237]
	v_pk_add_f32 v[24:25], v[24:25], v[234:235]
	v_pk_mul_f32 v[38:39], v[38:39], v[204:205] op_sel_hi:[1,0]
	v_pk_mul_f32 v[36:37], v[36:37], v[204:205] op_sel_hi:[1,0]
	v_pk_mul_f32 v[34:35], v[34:35], v[204:205] op_sel_hi:[1,0]
	v_pk_mul_f32 v[32:33], v[32:33], v[204:205] op_sel_hi:[1,0]
	v_pk_mul_f32 v[30:31], v[30:31], v[204:205] op_sel_hi:[1,0]
	v_pk_mul_f32 v[28:29], v[28:29], v[204:205] op_sel_hi:[1,0]
	v_pk_mul_f32 v[210:211], v[26:27], v[204:205] op_sel_hi:[1,0]
	v_pk_mul_f32 v[208:209], v[24:25], v[204:205] op_sel_hi:[1,0]
	v_cvt_pk_bf16_f32 v24, v36, v37
	v_cvt_pk_bf16_f32 v25, v38, v39
	v_cvt_pk_bf16_f32 v26, v32, v33
	v_cvt_pk_bf16_f32 v27, v34, v35
	v_cvt_pk_bf16_f32 v28, v28, v29
	v_cvt_pk_bf16_f32 v29, v30, v31
	v_cvt_pk_bf16_f32 v30, v208, v209
	v_cvt_pk_bf16_f32 v31, v210, v211
	v_cmp_lt_i32_e32 vcc, -1, v188
	s_and_saveexec_b64 s[38:39], vcc
	global_store_dwordx4 v[152:153], v[24:27], off
	global_store_dwordx4 v[152:153], v[28:31], off offset:256
	s_or_b64 exec, exec, s[38:39]
	v_pk_add_f32 v[20:21], v[20:21], v[248:249]
	v_pk_add_f32 v[18:19], v[18:19], v[246:247]
	v_pk_add_f32 v[16:17], v[16:17], v[244:245]
	v_pk_add_f32 v[14:15], v[14:15], v[242:243]
	v_pk_add_f32 v[12:13], v[12:13], v[240:241]
	v_pk_add_f32 v[10:11], v[10:11], v[238:239]
	v_pk_add_f32 v[8:9], v[8:9], v[236:237]
	v_pk_add_f32 v[6:7], v[6:7], v[234:235]
	v_pk_mul_f32 v[20:21], v[20:21], v[206:207] op_sel_hi:[1,0]
	v_pk_mul_f32 v[18:19], v[18:19], v[206:207] op_sel_hi:[1,0]
	v_pk_mul_f32 v[16:17], v[16:17], v[206:207] op_sel_hi:[1,0]
	v_pk_mul_f32 v[14:15], v[14:15], v[206:207] op_sel_hi:[1,0]
	v_pk_mul_f32 v[12:13], v[12:13], v[206:207] op_sel_hi:[1,0]
	v_pk_mul_f32 v[10:11], v[10:11], v[206:207] op_sel_hi:[1,0]
	v_pk_mul_f32 v[210:211], v[8:9], v[206:207] op_sel_hi:[1,0]
	v_pk_mul_f32 v[208:209], v[6:7], v[206:207] op_sel_hi:[1,0]
	v_cvt_pk_bf16_f32 v6, v18, v19
	v_cvt_pk_bf16_f32 v7, v20, v21
	v_cvt_pk_bf16_f32 v8, v14, v15
	v_cvt_pk_bf16_f32 v9, v16, v17
	v_cvt_pk_bf16_f32 v10, v10, v11
	v_cvt_pk_bf16_f32 v11, v12, v13
	v_cvt_pk_bf16_f32 v12, v208, v209
	v_cvt_pk_bf16_f32 v13, v210, v211
	v_cmp_lt_i32_e32 vcc, -1, v190
	s_and_saveexec_b64 s[38:39], vcc
	global_store_dwordx4 v[154:155], v[6:9], off
	global_store_dwordx4 v[154:155], v[10:13], off offset:256
